# mixer-B loop copies: loop-control SALU (stride add, counter add, compare) moved from behind the closing barrier into a PV MFMA gap; only the branch stays at the softmax-section head
# speedup vs baseline: 1.0080x; 1.0080x over previous
; #define ATT_SBAR() __builtin_amdgcn_sched_barrier(0)
; __device__ __forceinline__ unsigned cvtpk(float lo, float hi) { f32x2_t v = {lo, hi}; bf16x2_t b = __builtin_convertvector(v, bf16x2_t); return __builtin_bit_cast(unsigned, b); }
; #define ATT_LOAD_K(t) do { const unsigned so_ = (unsigned)(t) * (unsigned)(KVBLK * LDK * 2); sk0 = __builtin_bit_cast(bf16x8, __builtin_amdgcn_raw_buffer_load_b128(krs, koff, so_, 0)); \
;     if constexpr (DQK == 128) sk1 = __builtin_bit_cast(bf16x8, __builtin_amdgcn_raw_buffer_load_b128(krs, koff, so_ + (unsigned)(32 * LDK * 2), 0)); } while (0)
; #define ATT_LOAD_V(t) do { const unsigned so_ = (unsigned)(t) * (unsigned)(KVBLK * LDV * 2); sv0 = __builtin_bit_cast(bf16x8, __builtin_amdgcn_raw_buffer_load_b128(vrs, voff, so_, 0)); \
;     sv1 = __builtin_bit_cast(bf16x8, __builtin_amdgcn_raw_buffer_load_b128(vrs, voff, so_ + (unsigned)(32 * LDV * 2), 0)); } while (0)
; #define ATT_WRITE_K(so) do { *(bf16x8*)(K_lds + (so) + kswz<DQK>(kr, kc * 2)) = sk0; if constexpr (DQK == 128) *(bf16x8*)(K_lds + (so) + kswz<DQK>(32 + kr, kc * 2)) = sk1; } while (0)
;     ...
;   for (int t = 0; t + 1 < NT; ++t) {
;     if constexpr (ABL & 1) { u32x4 w0 = {cvtpk(p0[0], p0[1]), cvtpk(p0[2], p0[3]), cvtpk(p0[4], p0[5]), cvtpk(p0[6], p0[7])}, w1 = {cvtpk(p0[8], p0[9]), cvtpk(p0[10], p0[11]), cvtpk(p0[12], p0[13]), cvtpk(p0[14], p0[15])};
;         u32x4 w2 = {cvtpk(p1[0], p1[1]), cvtpk(p1[2], p1[3]), cvtpk(p1[4], p1[5]), cvtpk(p1[6], p1[7])}, w3 = {cvtpk(p1[8], p1[9]), cvtpk(p1[10], p1[11]), cvtpk(p1[12], p1[13]), cvtpk(p1[14], p1[15])};
;         pa0 = *reinterpret_cast<bf16x8*>(&w0); pa1 = *reinterpret_cast<bf16x8*>(&w1); pa2 = *reinterpret_cast<bf16x8*>(&w2); pa3 = *reinterpret_cast<bf16x8*>(&w3); }
;     else { ATT_SOFTMAX(t == 0); }
;     if constexpr (!(ABL & 4)) { ATT_WRITE_K(k2); ATT_WRITE_V(v1); }
;     ATT_SBAR();
; #pragma unroll
;     for (int ks = 0; ks < 4; ++ks) ATT_VPAIR(va, v0, 0, ks);
;     asm volatile("s_waitcnt lgkmcnt(8)" ::: "memory"); ATT_BAR();
;     ATT_XSECTION(true);
;     if constexpr (!(ABL & 4)) { const int tk = (t + 3 < NT) ? t + 3 : NT - 1, tv = (t + 2 < NT) ? t + 2 : NT - 1; ATT_LOAD_K(tk); ATT_LOAD_V(tv); }
;     ATT_BAR();
;     { const int tk_ = k0; k0 = k1; k1 = k2; k2 = tk_; const int tv_ = v0; v0 = v1; v1 = v2; v2 = tv_; }
;   }
.LBB0_283:
	v_exp_f32_e32 v98, v98
	v_exp_f32_e32 v114, v114
	v_exp_f32_e32 v99, v99
	v_exp_f32_e32 v115, v115
	v_exp_f32_e32 v100, v100
	v_exp_f32_e32 v101, v101
	v_exp_f32_e32 v102, v102
	v_exp_f32_e32 v103, v103
	v_exp_f32_e32 v106, v106
	v_exp_f32_e32 v107, v107
	v_exp_f32_e32 v116, v116
	v_exp_f32_e32 v117, v117
	v_exp_f32_e32 v118, v118
	v_exp_f32_e32 v119, v119
	v_exp_f32_e32 v104, v104
	v_exp_f32_e32 v120, v120
	v_exp_f32_e32 v105, v105
	v_exp_f32_e32 v121, v121
	v_exp_f32_e32 v122, v122
	v_exp_f32_e32 v123, v123
	v_exp_f32_e32 v108, v108
	v_exp_f32_e32 v124, v124
	v_exp_f32_e32 v109, v109
	v_exp_f32_e32 v125, v125
	v_exp_f32_e32 v110, v110
	v_exp_f32_e32 v126, v126
	v_exp_f32_e32 v111, v111
	v_exp_f32_e32 v127, v127
	v_exp_f32_e32 v112, v112
	v_exp_f32_e32 v128, v128
	v_exp_f32_e32 v113, v113
	v_exp_f32_e32 v129, v129
	v_cvt_pk_bf16_f32 v2, v98, v99
	v_cvt_pk_bf16_f32 v3, v100, v101
	v_cvt_pk_bf16_f32 v4, v102, v103
	v_cvt_pk_bf16_f32 v6, v106, v107
	v_cvt_pk_bf16_f32 v10, v114, v115
	v_cvt_pk_bf16_f32 v5, v104, v105
	v_cvt_pk_bf16_f32 v7, v108, v109
	v_cvt_pk_bf16_f32 v8, v110, v111
	v_cvt_pk_bf16_f32 v9, v112, v113
	v_cvt_pk_bf16_f32 v11, v116, v117
	v_cvt_pk_bf16_f32 v12, v118, v119
	v_cvt_pk_bf16_f32 v13, v120, v121
	v_cvt_pk_bf16_f32 v14, v122, v123
	v_cvt_pk_bf16_f32 v15, v124, v125
	v_cvt_pk_bf16_f32 v16, v126, v127
	v_cvt_pk_bf16_f32 v17, v128, v129
	s_waitcnt vmcnt(0)
	ds_write_b128 v248, v[224:227] offset:16384
	ds_write_b128 v167, v[228:231] offset:32768
	ds_write_b128 v168, v[232:235] offset:32768
	ds_read_b128 v[152:155], v249 offset:34816
	ds_read_b128 v[156:159], v249 offset:39424
	ds_read_b128 v[160:163], v249 offset:34848
	ds_read_b128 v[176:179], v249 offset:39456
	s_waitcnt lgkmcnt(4)
	s_barrier
	s_setprio 2
	s_waitcnt lgkmcnt(3)
	v_mfma_f32_32x32x16_bf16 v[98:113], v[152:155], v[136:139], v[82:97]
	ds_read_b128 v[180:183], v249 offset:34880
	s_waitcnt lgkmcnt(3)
	v_mfma_f32_32x32x16_bf16 v[114:129], v[156:159], v[136:139], v[82:97]
	ds_read_b128 v[186:189], v249 offset:39488
	s_waitcnt lgkmcnt(3)
	v_mfma_f32_32x32x16_bf16 v[98:113], v[160:163], v[140:143], v[98:113]
	ds_read_b128 v[190:193], v249 offset:34912
	ds_read_b64_tr_b16 v[198:199], v131 offset:16384
	ds_read_b64_tr_b16 v[200:201], v131 offset:18432
	s_waitcnt lgkmcnt(5)
	v_mfma_f32_32x32x16_bf16 v[114:129], v[176:179], v[140:143], v[114:129]
	ds_read_b128 v[194:197], v249 offset:39520
	ds_read_b64_tr_b16 v[212:213], v131 offset:20480
	ds_read_b64_tr_b16 v[214:215], v131 offset:22528
	s_waitcnt lgkmcnt(7)
	v_mfma_f32_32x32x16_bf16 v[98:113], v[180:183], v[144:147], v[98:113]
	ds_read_b64_tr_b16 v[216:217], v131 offset:24576
	ds_read_b64_tr_b16 v[218:219], v131 offset:26624
	s_waitcnt lgkmcnt(8)
	v_mfma_f32_32x32x16_bf16 v[114:129], v[186:189], v[144:147], v[114:129]
	ds_read_b64_tr_b16 v[220:221], v131 offset:28672
	ds_read_b64_tr_b16 v[222:223], v131 offset:30720
	s_waitcnt lgkmcnt(9)
	v_mfma_f32_32x32x16_bf16 v[98:113], v[190:193], v[148:151], v[98:113]
	s_waitcnt lgkmcnt(6)
	v_mfma_f32_32x32x16_bf16 v[114:129], v[194:197], v[148:151], v[114:129]
	v_mfma_f32_32x32x16_bf16 v[18:33], v[2:5], v[198:201], v[18:33]
	ds_read_b64_tr_b16 v[236:237], v131 offset:16896
	ds_read_b64_tr_b16 v[238:239], v131 offset:18944
	s_waitcnt lgkmcnt(6)
	v_mfma_f32_32x32x16_bf16 v[18:33], v[6:9], v[212:215], v[18:33]
	ds_read_b64_tr_b16 v[198:199], v131 offset:20992
	ds_read_b64_tr_b16 v[200:201], v131 offset:23040
	s_waitcnt lgkmcnt(6)
	v_mfma_f32_32x32x16_bf16 v[18:33], v[10:13], v[216:219], v[18:33]
	ds_read_b64_tr_b16 v[212:213], v131 offset:25088
	ds_read_b64_tr_b16 v[214:215], v131 offset:27136
	s_waitcnt lgkmcnt(6)
	v_mfma_f32_32x32x16_bf16 v[18:33], v[14:17], v[220:223], v[18:33]
	ds_read_b64_tr_b16 v[216:217], v131 offset:29184
	ds_read_b64_tr_b16 v[218:219], v131 offset:31232
	v_max3_f32 v152, v98, v99, v100
	s_waitcnt lgkmcnt(6)
	v_mfma_f32_32x32x16_bf16 v[34:49], v[2:5], v[236:239], v[34:49]
	ds_read_b64_tr_b16 v[220:221], v131 offset:17408
	ds_read_b64_tr_b16 v[222:223], v131 offset:19456
	v_max3_f32 v173, v114, v115, v116
	s_waitcnt lgkmcnt(6)
	v_mfma_f32_32x32x16_bf16 v[34:49], v[6:9], v[198:201], v[34:49]
	ds_read_b64_tr_b16 v[236:237], v131 offset:21504
	ds_read_b64_tr_b16 v[238:239], v131 offset:23552
	v_max3_f32 v152, v152, v101, v102
	s_waitcnt lgkmcnt(6)
	v_mfma_f32_32x32x16_bf16 v[34:49], v[10:13], v[212:215], v[34:49]
	ds_read_b64_tr_b16 v[198:199], v131 offset:25600
	ds_read_b64_tr_b16 v[200:201], v131 offset:27648
	v_max3_f32 v173, v173, v117, v118
	s_waitcnt lgkmcnt(6)
	v_mfma_f32_32x32x16_bf16 v[34:49], v[14:17], v[216:219], v[34:49]
	ds_read_b64_tr_b16 v[212:213], v131 offset:29696
	ds_read_b64_tr_b16 v[214:215], v131 offset:31744
	v_max3_f32 v152, v152, v103, v104
	s_waitcnt lgkmcnt(6)
	v_mfma_f32_32x32x16_bf16 v[50:65], v[2:5], v[220:223], v[50:65]
	ds_read_b64_tr_b16 v[216:217], v131 offset:17920
	ds_read_b64_tr_b16 v[218:219], v131 offset:19968
	v_max3_f32 v173, v173, v119, v120
	s_waitcnt lgkmcnt(6)
	v_mfma_f32_32x32x16_bf16 v[50:65], v[6:9], v[236:239], v[50:65]
	ds_read_b64_tr_b16 v[220:221], v131 offset:22016
	ds_read_b64_tr_b16 v[222:223], v131 offset:24064
	v_max3_f32 v152, v152, v105, v106
	s_waitcnt lgkmcnt(6)
	v_mfma_f32_32x32x16_bf16 v[50:65], v[10:13], v[198:201], v[50:65]
	ds_read_b64_tr_b16 v[236:237], v131 offset:26112
	ds_read_b64_tr_b16 v[238:239], v131 offset:28160
	v_max3_f32 v173, v173, v121, v122
	s_waitcnt lgkmcnt(6)
	v_mfma_f32_32x32x16_bf16 v[50:65], v[14:17], v[212:215], v[50:65]
	ds_read_b64_tr_b16 v[198:199], v131 offset:30208
	ds_read_b64_tr_b16 v[200:201], v131 offset:32256
	v_max3_f32 v152, v152, v107, v108
	s_waitcnt lgkmcnt(6)
	v_mfma_f32_32x32x16_bf16 v[66:81], v[2:5], v[216:219], v[66:81]
	v_max3_f32 v173, v173, v123, v124
	s_min_u32 s14, s97, 0x7c
	s_lshl_b32 s14, s14, 17
	s_add_i32 s14, s14, 0x60000
	buffer_load_dwordx4 v[224:227], v170, s[8:11], s14 offen
	s_waitcnt lgkmcnt(4)
	v_mfma_f32_32x32x16_bf16 v[66:81], v[6:9], v[220:223], v[66:81]
	v_max3_f32 v152, v152, v109, v110
	s_add_i32 s19, s36, 0xffff0000
	s_mov_b32 s14, s10
	s_mov_b32 s15, s11
	buffer_load_dwordx4 v[228:231], v171, s[12:15], s19 offen
	s_waitcnt lgkmcnt(2)
	v_mfma_f32_32x32x16_bf16 v[66:81], v[10:13], v[236:239], v[66:81]
	v_max3_f32 v173, v173, v125, v126
	buffer_load_dwordx4 v[232:235], v171, s[12:15], s36 offen
	s_add_i32 s36, s36, 0x20000
	s_add_i32 s97, s97, 1
	s_cmpk_eq_i32 s97, 0x7e
	s_waitcnt lgkmcnt(0)
	v_mfma_f32_32x32x16_bf16 v[66:81], v[14:17], v[198:201], v[66:81]
	v_max3_f32 v152, v152, v111, v112
	v_mfma_f32_16x16x32_bf16 v[240:243], v[2:5], v[132:135], v[240:243]
	v_max3_f32 v173, v173, v127, v128
	v_mfma_f32_16x16x32_bf16 v[240:243], v[6:9], v[132:135], v[240:243]
	v_max_f32 v152, v152, v113
	v_mfma_f32_16x16x32_bf16 v[240:243], v[10:13], v[132:135], v[240:243]
	v_max_f32 v173, v173, v129
	v_mfma_f32_16x16x32_bf16 v[240:243], v[14:17], v[132:135], v[240:243]
	v_max_f32 v173, v173, v152
	s_setprio 0
	s_barrier
	s_cbranch_scc1 .Lu3_exit_b1_0

; #define ATT_SBAR() __builtin_amdgcn_sched_barrier(0)
; __device__ __forceinline__ unsigned cvtpk(float lo, float hi) { f32x2_t v = {lo, hi}; bf16x2_t b = __builtin_convertvector(v, bf16x2_t); return __builtin_bit_cast(unsigned, b); }
; #define ATT_LOAD_K(t) do { const unsigned so_ = (unsigned)(t) * (unsigned)(KVBLK * LDK * 2); sk0 = __builtin_bit_cast(bf16x8, __builtin_amdgcn_raw_buffer_load_b128(krs, koff, so_, 0)); \
;     if constexpr (DQK == 128) sk1 = __builtin_bit_cast(bf16x8, __builtin_amdgcn_raw_buffer_load_b128(krs, koff, so_ + (unsigned)(32 * LDK * 2), 0)); } while (0)
; #define ATT_LOAD_V(t) do { const unsigned so_ = (unsigned)(t) * (unsigned)(KVBLK * LDV * 2); sv0 = __builtin_bit_cast(bf16x8, __builtin_amdgcn_raw_buffer_load_b128(vrs, voff, so_, 0)); \
;     sv1 = __builtin_bit_cast(bf16x8, __builtin_amdgcn_raw_buffer_load_b128(vrs, voff, so_ + (unsigned)(32 * LDV * 2), 0)); } while (0)
; #define ATT_WRITE_K(so) do { *(bf16x8*)(K_lds + (so) + kswz<DQK>(kr, kc * 2)) = sk0; if constexpr (DQK == 128) *(bf16x8*)(K_lds + (so) + kswz<DQK>(32 + kr, kc * 2)) = sk1; } while (0)
;     ...
;   for (int t = 0; t + 1 < NT; ++t) {
;     if constexpr (ABL & 1) { u32x4 w0 = {cvtpk(p0[0], p0[1]), cvtpk(p0[2], p0[3]), cvtpk(p0[4], p0[5]), cvtpk(p0[6], p0[7])}, w1 = {cvtpk(p0[8], p0[9]), cvtpk(p0[10], p0[11]), cvtpk(p0[12], p0[13]), cvtpk(p0[14], p0[15])};
;         u32x4 w2 = {cvtpk(p1[0], p1[1]), cvtpk(p1[2], p1[3]), cvtpk(p1[4], p1[5]), cvtpk(p1[6], p1[7])}, w3 = {cvtpk(p1[8], p1[9]), cvtpk(p1[10], p1[11]), cvtpk(p1[12], p1[13]), cvtpk(p1[14], p1[15])};
;         pa0 = *reinterpret_cast<bf16x8*>(&w0); pa1 = *reinterpret_cast<bf16x8*>(&w1); pa2 = *reinterpret_cast<bf16x8*>(&w2); pa3 = *reinterpret_cast<bf16x8*>(&w3); }
;     else { ATT_SOFTMAX(t == 0); }
;     if constexpr (!(ABL & 4)) { ATT_WRITE_K(k2); ATT_WRITE_V(v1); }
;     ATT_SBAR();
; #pragma unroll
;     for (int ks = 0; ks < 4; ++ks) ATT_VPAIR(va, v0, 0, ks);
;     asm volatile("s_waitcnt lgkmcnt(8)" ::: "memory"); ATT_BAR();
;     ATT_XSECTION(true);
;     if constexpr (!(ABL & 4)) { const int tk = (t + 3 < NT) ? t + 3 : NT - 1, tv = (t + 2 < NT) ? t + 2 : NT - 1; ATT_LOAD_K(tk); ATT_LOAD_V(tv); }
;     ATT_BAR();
;     { const int tk_ = k0; k0 = k1; k1 = k2; k2 = tk_; const int tv_ = v0; v0 = v1; v1 = v2; v2 = tv_; }
;   }
.Lu3_join_b1_1:
	v_exp_f32_e32 v98, v98
	v_exp_f32_e32 v114, v114
	v_exp_f32_e32 v99, v99
	v_exp_f32_e32 v115, v115
	v_exp_f32_e32 v100, v100
	v_exp_f32_e32 v101, v101
	v_exp_f32_e32 v102, v102
	v_exp_f32_e32 v103, v103
	v_exp_f32_e32 v106, v106
	v_exp_f32_e32 v107, v107
	v_exp_f32_e32 v116, v116
	v_exp_f32_e32 v117, v117
	v_exp_f32_e32 v118, v118
	v_exp_f32_e32 v119, v119
	v_exp_f32_e32 v104, v104
	v_exp_f32_e32 v120, v120
	v_exp_f32_e32 v105, v105
	v_exp_f32_e32 v121, v121
	v_exp_f32_e32 v122, v122
	v_exp_f32_e32 v123, v123
	v_exp_f32_e32 v108, v108
	v_exp_f32_e32 v124, v124
	v_exp_f32_e32 v109, v109
	v_exp_f32_e32 v125, v125
	v_exp_f32_e32 v110, v110
	v_exp_f32_e32 v126, v126
	v_exp_f32_e32 v111, v111
	v_exp_f32_e32 v127, v127
	v_exp_f32_e32 v112, v112
	v_exp_f32_e32 v128, v128
	v_exp_f32_e32 v113, v113
	v_exp_f32_e32 v129, v129
	v_cvt_pk_bf16_f32 v2, v98, v99
	v_cvt_pk_bf16_f32 v3, v100, v101
	v_cvt_pk_bf16_f32 v4, v102, v103
	v_cvt_pk_bf16_f32 v6, v106, v107
	v_cvt_pk_bf16_f32 v10, v114, v115
	v_cvt_pk_bf16_f32 v5, v104, v105
	v_cvt_pk_bf16_f32 v7, v108, v109
	v_cvt_pk_bf16_f32 v8, v110, v111
	v_cvt_pk_bf16_f32 v9, v112, v113
	v_cvt_pk_bf16_f32 v11, v116, v117
	v_cvt_pk_bf16_f32 v12, v118, v119
	v_cvt_pk_bf16_f32 v13, v120, v121
	v_cvt_pk_bf16_f32 v14, v122, v123
	v_cvt_pk_bf16_f32 v15, v124, v125
	v_cvt_pk_bf16_f32 v16, v126, v127
	v_cvt_pk_bf16_f32 v17, v128, v129
	s_waitcnt vmcnt(0)
	ds_write_b128 v248, v[224:227] offset:25600
	ds_write_b128 v167, v[228:231]
	ds_write_b128 v168, v[232:235]
	ds_read_b128 v[152:155], v249 offset:16384
	ds_read_b128 v[156:159], v249 offset:20992
	ds_read_b128 v[160:163], v249 offset:16416
	ds_read_b128 v[176:179], v249 offset:21024
	s_waitcnt lgkmcnt(4)
	s_barrier
	s_setprio 2
	s_waitcnt lgkmcnt(3)
	v_mfma_f32_32x32x16_bf16 v[98:113], v[152:155], v[136:139], v[82:97]
	ds_read_b128 v[180:183], v249 offset:16448
	s_waitcnt lgkmcnt(3)
	v_mfma_f32_32x32x16_bf16 v[114:129], v[156:159], v[136:139], v[82:97]
	ds_read_b128 v[186:189], v249 offset:21056
	s_waitcnt lgkmcnt(3)
	v_mfma_f32_32x32x16_bf16 v[98:113], v[160:163], v[140:143], v[98:113]
	ds_read_b128 v[190:193], v249 offset:16480
	ds_read_b64_tr_b16 v[198:199], v131 offset:32768
	ds_read_b64_tr_b16 v[200:201], v131 offset:34816
	s_waitcnt lgkmcnt(5)
	v_mfma_f32_32x32x16_bf16 v[114:129], v[176:179], v[140:143], v[114:129]
	ds_read_b128 v[194:197], v249 offset:21088
	ds_read_b64_tr_b16 v[212:213], v131 offset:36864
	ds_read_b64_tr_b16 v[214:215], v131 offset:38912
	s_waitcnt lgkmcnt(7)
	v_mfma_f32_32x32x16_bf16 v[98:113], v[180:183], v[144:147], v[98:113]
	ds_read_b64_tr_b16 v[216:217], v131 offset:40960
	ds_read_b64_tr_b16 v[218:219], v131 offset:43008
	s_waitcnt lgkmcnt(8)
	v_mfma_f32_32x32x16_bf16 v[114:129], v[186:189], v[144:147], v[114:129]
	ds_read_b64_tr_b16 v[220:221], v131 offset:45056
	ds_read_b64_tr_b16 v[222:223], v131 offset:47104
	s_waitcnt lgkmcnt(9)
	v_mfma_f32_32x32x16_bf16 v[98:113], v[190:193], v[148:151], v[98:113]
	s_waitcnt lgkmcnt(6)
	v_mfma_f32_32x32x16_bf16 v[114:129], v[194:197], v[148:151], v[114:129]
	v_mfma_f32_32x32x16_bf16 v[18:33], v[2:5], v[198:201], v[18:33]
	ds_read_b64_tr_b16 v[236:237], v131 offset:33280
	ds_read_b64_tr_b16 v[238:239], v131 offset:35328
	s_waitcnt lgkmcnt(6)
	v_mfma_f32_32x32x16_bf16 v[18:33], v[6:9], v[212:215], v[18:33]
	ds_read_b64_tr_b16 v[198:199], v131 offset:37376
	ds_read_b64_tr_b16 v[200:201], v131 offset:39424
	s_waitcnt lgkmcnt(6)
	v_mfma_f32_32x32x16_bf16 v[18:33], v[10:13], v[216:219], v[18:33]
	ds_read_b64_tr_b16 v[212:213], v131 offset:41472
	ds_read_b64_tr_b16 v[214:215], v131 offset:43520
	s_waitcnt lgkmcnt(6)
	v_mfma_f32_32x32x16_bf16 v[18:33], v[14:17], v[220:223], v[18:33]
	ds_read_b64_tr_b16 v[216:217], v131 offset:45568
	ds_read_b64_tr_b16 v[218:219], v131 offset:47616
	v_max3_f32 v152, v98, v99, v100
	s_waitcnt lgkmcnt(6)
	v_mfma_f32_32x32x16_bf16 v[34:49], v[2:5], v[236:239], v[34:49]
	ds_read_b64_tr_b16 v[220:221], v131 offset:33792
	ds_read_b64_tr_b16 v[222:223], v131 offset:35840
	v_max3_f32 v173, v114, v115, v116
	s_waitcnt lgkmcnt(6)
	v_mfma_f32_32x32x16_bf16 v[34:49], v[6:9], v[198:201], v[34:49]
	ds_read_b64_tr_b16 v[236:237], v131 offset:37888
	ds_read_b64_tr_b16 v[238:239], v131 offset:39936
	v_max3_f32 v152, v152, v101, v102
	s_waitcnt lgkmcnt(6)
	v_mfma_f32_32x32x16_bf16 v[34:49], v[10:13], v[212:215], v[34:49]
	ds_read_b64_tr_b16 v[198:199], v131 offset:41984
	ds_read_b64_tr_b16 v[200:201], v131 offset:44032
	v_max3_f32 v173, v173, v117, v118
	s_waitcnt lgkmcnt(6)
	v_mfma_f32_32x32x16_bf16 v[34:49], v[14:17], v[216:219], v[34:49]
	ds_read_b64_tr_b16 v[212:213], v131 offset:46080
	ds_read_b64_tr_b16 v[214:215], v131 offset:48128
	v_max3_f32 v152, v152, v103, v104
	s_waitcnt lgkmcnt(6)
	v_mfma_f32_32x32x16_bf16 v[50:65], v[2:5], v[220:223], v[50:65]
	ds_read_b64_tr_b16 v[216:217], v131 offset:34304
	ds_read_b64_tr_b16 v[218:219], v131 offset:36352
	v_max3_f32 v173, v173, v119, v120
	s_waitcnt lgkmcnt(6)
	v_mfma_f32_32x32x16_bf16 v[50:65], v[6:9], v[236:239], v[50:65]
	ds_read_b64_tr_b16 v[220:221], v131 offset:38400
	ds_read_b64_tr_b16 v[222:223], v131 offset:40448
	v_max3_f32 v152, v152, v105, v106
	s_waitcnt lgkmcnt(6)
	v_mfma_f32_32x32x16_bf16 v[50:65], v[10:13], v[198:201], v[50:65]
	ds_read_b64_tr_b16 v[236:237], v131 offset:42496
	ds_read_b64_tr_b16 v[238:239], v131 offset:44544
	v_max3_f32 v173, v173, v121, v122
	s_waitcnt lgkmcnt(6)
	v_mfma_f32_32x32x16_bf16 v[50:65], v[14:17], v[212:215], v[50:65]
	ds_read_b64_tr_b16 v[198:199], v131 offset:46592
	ds_read_b64_tr_b16 v[200:201], v131 offset:48640
	v_max3_f32 v152, v152, v107, v108
	s_waitcnt lgkmcnt(6)
	v_mfma_f32_32x32x16_bf16 v[66:81], v[2:5], v[216:219], v[66:81]
	v_max3_f32 v173, v173, v123, v124
	s_min_u32 s14, s97, 0x7c
	s_lshl_b32 s14, s14, 17
	s_add_i32 s14, s14, 0x60000
	buffer_load_dwordx4 v[224:227], v170, s[8:11], s14 offen
	s_waitcnt lgkmcnt(4)
	v_mfma_f32_32x32x16_bf16 v[66:81], v[6:9], v[220:223], v[66:81]
	v_max3_f32 v152, v152, v109, v110
	s_add_i32 s19, s36, 0xffff0000
	s_mov_b32 s14, s10
	s_mov_b32 s15, s11
	buffer_load_dwordx4 v[228:231], v171, s[12:15], s19 offen
	s_waitcnt lgkmcnt(2)
	v_mfma_f32_32x32x16_bf16 v[66:81], v[10:13], v[236:239], v[66:81]
	v_max3_f32 v173, v173, v125, v126
	buffer_load_dwordx4 v[232:235], v171, s[12:15], s36 offen
	s_add_i32 s36, s36, 0x20000
	s_add_i32 s97, s97, 1
	s_cmpk_eq_i32 s97, 0x7e
	s_waitcnt lgkmcnt(0)
	v_mfma_f32_32x32x16_bf16 v[66:81], v[14:17], v[198:201], v[66:81]
	v_max3_f32 v152, v152, v111, v112
	v_mfma_f32_16x16x32_bf16 v[240:243], v[2:5], v[132:135], v[240:243]
	v_max3_f32 v173, v173, v127, v128
	v_mfma_f32_16x16x32_bf16 v[240:243], v[6:9], v[132:135], v[240:243]
	v_max_f32 v152, v152, v113
	v_mfma_f32_16x16x32_bf16 v[240:243], v[10:13], v[132:135], v[240:243]
	v_max_f32 v173, v173, v129
	v_mfma_f32_16x16x32_bf16 v[240:243], v[14:17], v[132:135], v[240:243]
	v_max_f32 v173, v173, v152
	s_setprio 0
	s_barrier
	s_cbranch_scc1 .Lu3_exit_b1_1

; #define ATT_SBAR() __builtin_amdgcn_sched_barrier(0)
; __device__ __forceinline__ unsigned cvtpk(float lo, float hi) { f32x2_t v = {lo, hi}; bf16x2_t b = __builtin_convertvector(v, bf16x2_t); return __builtin_bit_cast(unsigned, b); }
; #define ATT_LOAD_K(t) do { const unsigned so_ = (unsigned)(t) * (unsigned)(KVBLK * LDK * 2); sk0 = __builtin_bit_cast(bf16x8, __builtin_amdgcn_raw_buffer_load_b128(krs, koff, so_, 0)); \
;     if constexpr (DQK == 128) sk1 = __builtin_bit_cast(bf16x8, __builtin_amdgcn_raw_buffer_load_b128(krs, koff, so_ + (unsigned)(32 * LDK * 2), 0)); } while (0)
; #define ATT_LOAD_V(t) do { const unsigned so_ = (unsigned)(t) * (unsigned)(KVBLK * LDV * 2); sv0 = __builtin_bit_cast(bf16x8, __builtin_amdgcn_raw_buffer_load_b128(vrs, voff, so_, 0)); \
;     sv1 = __builtin_bit_cast(bf16x8, __builtin_amdgcn_raw_buffer_load_b128(vrs, voff, so_ + (unsigned)(32 * LDV * 2), 0)); } while (0)
; #define ATT_WRITE_K(so) do { *(bf16x8*)(K_lds + (so) + kswz<DQK>(kr, kc * 2)) = sk0; if constexpr (DQK == 128) *(bf16x8*)(K_lds + (so) + kswz<DQK>(32 + kr, kc * 2)) = sk1; } while (0)
;     ...
;   for (int t = 0; t + 1 < NT; ++t) {
;     if constexpr (ABL & 1) { u32x4 w0 = {cvtpk(p0[0], p0[1]), cvtpk(p0[2], p0[3]), cvtpk(p0[4], p0[5]), cvtpk(p0[6], p0[7])}, w1 = {cvtpk(p0[8], p0[9]), cvtpk(p0[10], p0[11]), cvtpk(p0[12], p0[13]), cvtpk(p0[14], p0[15])};
;         u32x4 w2 = {cvtpk(p1[0], p1[1]), cvtpk(p1[2], p1[3]), cvtpk(p1[4], p1[5]), cvtpk(p1[6], p1[7])}, w3 = {cvtpk(p1[8], p1[9]), cvtpk(p1[10], p1[11]), cvtpk(p1[12], p1[13]), cvtpk(p1[14], p1[15])};
;         pa0 = *reinterpret_cast<bf16x8*>(&w0); pa1 = *reinterpret_cast<bf16x8*>(&w1); pa2 = *reinterpret_cast<bf16x8*>(&w2); pa3 = *reinterpret_cast<bf16x8*>(&w3); }
;     else { ATT_SOFTMAX(t == 0); }
;     if constexpr (!(ABL & 4)) { ATT_WRITE_K(k2); ATT_WRITE_V(v1); }
;     ATT_SBAR();
; #pragma unroll
;     for (int ks = 0; ks < 4; ++ks) ATT_VPAIR(va, v0, 0, ks);
;     asm volatile("s_waitcnt lgkmcnt(8)" ::: "memory"); ATT_BAR();
;     ATT_XSECTION(true);
;     if constexpr (!(ABL & 4)) { const int tk = (t + 3 < NT) ? t + 3 : NT - 1, tv = (t + 2 < NT) ? t + 2 : NT - 1; ATT_LOAD_K(tk); ATT_LOAD_V(tv); }
;     ATT_BAR();
;     { const int tk_ = k0; k0 = k1; k1 = k2; k2 = tk_; const int tv_ = v0; v0 = v1; v1 = v2; v2 = tv_; }
;   }
.Lu3_join_b1_2:
	v_exp_f32_e32 v98, v98
	v_exp_f32_e32 v114, v114
	v_exp_f32_e32 v99, v99
	v_exp_f32_e32 v115, v115
	v_exp_f32_e32 v100, v100
	v_exp_f32_e32 v101, v101
	v_exp_f32_e32 v102, v102
	v_exp_f32_e32 v103, v103
	v_exp_f32_e32 v106, v106
	v_exp_f32_e32 v107, v107
	v_exp_f32_e32 v116, v116
	v_exp_f32_e32 v117, v117
	v_exp_f32_e32 v118, v118
	v_exp_f32_e32 v119, v119
	v_exp_f32_e32 v104, v104
	v_exp_f32_e32 v120, v120
	v_exp_f32_e32 v105, v105
	v_exp_f32_e32 v121, v121
	v_exp_f32_e32 v122, v122
	v_exp_f32_e32 v123, v123
	v_exp_f32_e32 v108, v108
	v_exp_f32_e32 v124, v124
	v_exp_f32_e32 v109, v109
	v_exp_f32_e32 v125, v125
	v_exp_f32_e32 v110, v110
	v_exp_f32_e32 v126, v126
	v_exp_f32_e32 v111, v111
	v_exp_f32_e32 v127, v127
	v_exp_f32_e32 v112, v112
	v_exp_f32_e32 v128, v128
	v_exp_f32_e32 v113, v113
	v_exp_f32_e32 v129, v129
	v_cvt_pk_bf16_f32 v2, v98, v99
	v_cvt_pk_bf16_f32 v3, v100, v101
	v_cvt_pk_bf16_f32 v4, v102, v103
	v_cvt_pk_bf16_f32 v6, v106, v107
	v_cvt_pk_bf16_f32 v10, v114, v115
	v_cvt_pk_bf16_f32 v5, v104, v105
	v_cvt_pk_bf16_f32 v7, v108, v109
	v_cvt_pk_bf16_f32 v8, v110, v111
	v_cvt_pk_bf16_f32 v9, v112, v113
	v_cvt_pk_bf16_f32 v11, v116, v117
	v_cvt_pk_bf16_f32 v12, v118, v119
	v_cvt_pk_bf16_f32 v13, v120, v121
	v_cvt_pk_bf16_f32 v14, v122, v123
	v_cvt_pk_bf16_f32 v15, v124, v125
	v_cvt_pk_bf16_f32 v16, v126, v127
	v_cvt_pk_bf16_f32 v17, v128, v129
	s_waitcnt vmcnt(0)
	ds_write_b128 v248, v[224:227] offset:34816
	ds_write_b128 v167, v[228:231] offset:16384
	ds_write_b128 v168, v[232:235] offset:16384
	ds_read_b128 v[152:155], v249 offset:25600
	ds_read_b128 v[156:159], v249 offset:30208
	ds_read_b128 v[160:163], v249 offset:25632
	ds_read_b128 v[176:179], v249 offset:30240
	s_waitcnt lgkmcnt(4)
	s_barrier
	s_setprio 2
	s_waitcnt lgkmcnt(3)
	v_mfma_f32_32x32x16_bf16 v[98:113], v[152:155], v[136:139], v[82:97]
	ds_read_b128 v[180:183], v249 offset:25664
	s_waitcnt lgkmcnt(3)
	v_mfma_f32_32x32x16_bf16 v[114:129], v[156:159], v[136:139], v[82:97]
	ds_read_b128 v[186:189], v249 offset:30272
	s_waitcnt lgkmcnt(3)
	v_mfma_f32_32x32x16_bf16 v[98:113], v[160:163], v[140:143], v[98:113]
	ds_read_b128 v[190:193], v249 offset:25696
	ds_read_b64_tr_b16 v[198:199], v131
	ds_read_b64_tr_b16 v[200:201], v131 offset:2048
	s_waitcnt lgkmcnt(5)
	v_mfma_f32_32x32x16_bf16 v[114:129], v[176:179], v[140:143], v[114:129]
	ds_read_b128 v[194:197], v249 offset:30304
	ds_read_b64_tr_b16 v[212:213], v131 offset:4096
	ds_read_b64_tr_b16 v[214:215], v131 offset:6144
	s_waitcnt lgkmcnt(7)
	v_mfma_f32_32x32x16_bf16 v[98:113], v[180:183], v[144:147], v[98:113]
	ds_read_b64_tr_b16 v[216:217], v131 offset:8192
	ds_read_b64_tr_b16 v[218:219], v131 offset:10240
	s_waitcnt lgkmcnt(8)
	v_mfma_f32_32x32x16_bf16 v[114:129], v[186:189], v[144:147], v[114:129]
	ds_read_b64_tr_b16 v[220:221], v131 offset:12288
	ds_read_b64_tr_b16 v[222:223], v131 offset:14336
	s_waitcnt lgkmcnt(9)
	v_mfma_f32_32x32x16_bf16 v[98:113], v[190:193], v[148:151], v[98:113]
	s_waitcnt lgkmcnt(6)
	v_mfma_f32_32x32x16_bf16 v[114:129], v[194:197], v[148:151], v[114:129]
	v_mfma_f32_32x32x16_bf16 v[18:33], v[2:5], v[198:201], v[18:33]
	ds_read_b64_tr_b16 v[236:237], v131 offset:512
	ds_read_b64_tr_b16 v[238:239], v131 offset:2560
	s_waitcnt lgkmcnt(6)
	v_mfma_f32_32x32x16_bf16 v[18:33], v[6:9], v[212:215], v[18:33]
	ds_read_b64_tr_b16 v[198:199], v131 offset:4608
	ds_read_b64_tr_b16 v[200:201], v131 offset:6656
	s_waitcnt lgkmcnt(6)
	v_mfma_f32_32x32x16_bf16 v[18:33], v[10:13], v[216:219], v[18:33]
	ds_read_b64_tr_b16 v[212:213], v131 offset:8704
	ds_read_b64_tr_b16 v[214:215], v131 offset:10752
	s_waitcnt lgkmcnt(6)
	v_mfma_f32_32x32x16_bf16 v[18:33], v[14:17], v[220:223], v[18:33]
	ds_read_b64_tr_b16 v[216:217], v131 offset:12800
	ds_read_b64_tr_b16 v[218:219], v131 offset:14848
	v_max3_f32 v152, v98, v99, v100
	s_waitcnt lgkmcnt(6)
	v_mfma_f32_32x32x16_bf16 v[34:49], v[2:5], v[236:239], v[34:49]
	ds_read_b64_tr_b16 v[220:221], v131 offset:1024
	ds_read_b64_tr_b16 v[222:223], v131 offset:3072
	v_max3_f32 v173, v114, v115, v116
	s_waitcnt lgkmcnt(6)
	v_mfma_f32_32x32x16_bf16 v[34:49], v[6:9], v[198:201], v[34:49]
	ds_read_b64_tr_b16 v[236:237], v131 offset:5120
	ds_read_b64_tr_b16 v[238:239], v131 offset:7168
	v_max3_f32 v152, v152, v101, v102
	s_waitcnt lgkmcnt(6)
	v_mfma_f32_32x32x16_bf16 v[34:49], v[10:13], v[212:215], v[34:49]
	ds_read_b64_tr_b16 v[198:199], v131 offset:9216
	ds_read_b64_tr_b16 v[200:201], v131 offset:11264
	v_max3_f32 v173, v173, v117, v118
	s_waitcnt lgkmcnt(6)
	v_mfma_f32_32x32x16_bf16 v[34:49], v[14:17], v[216:219], v[34:49]
	ds_read_b64_tr_b16 v[212:213], v131 offset:13312
	ds_read_b64_tr_b16 v[214:215], v131 offset:15360
	v_max3_f32 v152, v152, v103, v104
	s_waitcnt lgkmcnt(6)
	v_mfma_f32_32x32x16_bf16 v[50:65], v[2:5], v[220:223], v[50:65]
	ds_read_b64_tr_b16 v[216:217], v131 offset:1536
	ds_read_b64_tr_b16 v[218:219], v131 offset:3584
	v_max3_f32 v173, v173, v119, v120
	s_waitcnt lgkmcnt(6)
	v_mfma_f32_32x32x16_bf16 v[50:65], v[6:9], v[236:239], v[50:65]
	ds_read_b64_tr_b16 v[220:221], v131 offset:5632
	ds_read_b64_tr_b16 v[222:223], v131 offset:7680
	v_max3_f32 v152, v152, v105, v106
	s_waitcnt lgkmcnt(6)
	v_mfma_f32_32x32x16_bf16 v[50:65], v[10:13], v[198:201], v[50:65]
	ds_read_b64_tr_b16 v[236:237], v131 offset:9728
	ds_read_b64_tr_b16 v[238:239], v131 offset:11776
	v_max3_f32 v173, v173, v121, v122
	s_waitcnt lgkmcnt(6)
	v_mfma_f32_32x32x16_bf16 v[50:65], v[14:17], v[212:215], v[50:65]
	ds_read_b64_tr_b16 v[198:199], v131 offset:13824
	ds_read_b64_tr_b16 v[200:201], v131 offset:15872
	v_max3_f32 v152, v152, v107, v108
	s_waitcnt lgkmcnt(6)
	v_mfma_f32_32x32x16_bf16 v[66:81], v[2:5], v[216:219], v[66:81]
	v_max3_f32 v173, v173, v123, v124
	s_min_u32 s14, s97, 0x7c
	s_lshl_b32 s14, s14, 17
	s_add_i32 s14, s14, 0x60000
	buffer_load_dwordx4 v[224:227], v170, s[8:11], s14 offen
	s_waitcnt lgkmcnt(4)
	v_mfma_f32_32x32x16_bf16 v[66:81], v[6:9], v[220:223], v[66:81]
	v_max3_f32 v152, v152, v109, v110
	s_add_i32 s19, s36, 0xffff0000
	s_mov_b32 s14, s10
	s_mov_b32 s15, s11
	buffer_load_dwordx4 v[228:231], v171, s[12:15], s19 offen
	s_waitcnt lgkmcnt(2)
	v_mfma_f32_32x32x16_bf16 v[66:81], v[10:13], v[236:239], v[66:81]
	v_max3_f32 v173, v173, v125, v126
	buffer_load_dwordx4 v[232:235], v171, s[12:15], s36 offen
	s_add_i32 s36, s36, 0x20000
	s_add_i32 s97, s97, 1
	s_cmpk_eq_i32 s97, 0x7e
	s_waitcnt lgkmcnt(0)
	v_mfma_f32_32x32x16_bf16 v[66:81], v[14:17], v[198:201], v[66:81]
	v_max3_f32 v152, v152, v111, v112
	v_mfma_f32_16x16x32_bf16 v[240:243], v[2:5], v[132:135], v[240:243]
	v_max3_f32 v173, v173, v127, v128
	v_mfma_f32_16x16x32_bf16 v[240:243], v[6:9], v[132:135], v[240:243]
	v_max_f32 v152, v152, v113
	v_mfma_f32_16x16x32_bf16 v[240:243], v[10:13], v[132:135], v[240:243]
	v_max_f32 v173, v173, v129
	v_mfma_f32_16x16x32_bf16 v[240:243], v[14:17], v[132:135], v[240:243]
	v_max_f32 v173, v173, v152
	s_setprio 0
	s_barrier
	s_cbranch_scc1 .Lu3_exit_b1_2
	s_branch .Lu3_b1_0

; #define ATT_SBAR() __builtin_amdgcn_sched_barrier(0)
; __device__ __forceinline__ unsigned cvtpk(float lo, float hi) { f32x2_t v = {lo, hi}; bf16x2_t b = __builtin_convertvector(v, bf16x2_t); return __builtin_bit_cast(unsigned, b); }
; #define ATT_LOAD_K(t) do { const unsigned so_ = (unsigned)(t) * (unsigned)(KVBLK * LDK * 2); sk0 = __builtin_bit_cast(bf16x8, __builtin_amdgcn_raw_buffer_load_b128(krs, koff, so_, 0)); \
;     if constexpr (DQK == 128) sk1 = __builtin_bit_cast(bf16x8, __builtin_amdgcn_raw_buffer_load_b128(krs, koff, so_ + (unsigned)(32 * LDK * 2), 0)); } while (0)
; #define ATT_LOAD_V(t) do { const unsigned so_ = (unsigned)(t) * (unsigned)(KVBLK * LDV * 2); sv0 = __builtin_bit_cast(bf16x8, __builtin_amdgcn_raw_buffer_load_b128(vrs, voff, so_, 0)); \
;     sv1 = __builtin_bit_cast(bf16x8, __builtin_amdgcn_raw_buffer_load_b128(vrs, voff, so_ + (unsigned)(32 * LDV * 2), 0)); } while (0)
; #define ATT_WRITE_K(so) do { *(bf16x8*)(K_lds + (so) + kswz<DQK>(kr, kc * 2)) = sk0; if constexpr (DQK == 128) *(bf16x8*)(K_lds + (so) + kswz<DQK>(32 + kr, kc * 2)) = sk1; } while (0)
;     ...
;   for (int t = 0; t + 1 < NT; ++t) {
;     if constexpr (ABL & 1) { u32x4 w0 = {cvtpk(p0[0], p0[1]), cvtpk(p0[2], p0[3]), cvtpk(p0[4], p0[5]), cvtpk(p0[6], p0[7])}, w1 = {cvtpk(p0[8], p0[9]), cvtpk(p0[10], p0[11]), cvtpk(p0[12], p0[13]), cvtpk(p0[14], p0[15])};
;         u32x4 w2 = {cvtpk(p1[0], p1[1]), cvtpk(p1[2], p1[3]), cvtpk(p1[4], p1[5]), cvtpk(p1[6], p1[7])}, w3 = {cvtpk(p1[8], p1[9]), cvtpk(p1[10], p1[11]), cvtpk(p1[12], p1[13]), cvtpk(p1[14], p1[15])};
;         pa0 = *reinterpret_cast<bf16x8*>(&w0); pa1 = *reinterpret_cast<bf16x8*>(&w1); pa2 = *reinterpret_cast<bf16x8*>(&w2); pa3 = *reinterpret_cast<bf16x8*>(&w3); }
;     else { ATT_SOFTMAX(t == 0); }
;     if constexpr (!(ABL & 4)) { ATT_WRITE_K(k2); ATT_WRITE_V(v1); }
;     ATT_SBAR();
; #pragma unroll
;     for (int ks = 0; ks < 4; ++ks) ATT_VPAIR(va, v0, 0, ks);
;     asm volatile("s_waitcnt lgkmcnt(8)" ::: "memory"); ATT_BAR();
;     ATT_XSECTION(true);
;     if constexpr (!(ABL & 4)) { const int tk = (t + 3 < NT) ? t + 3 : NT - 1, tv = (t + 2 < NT) ? t + 2 : NT - 1; ATT_LOAD_K(tk); ATT_LOAD_V(tv); }
;     ATT_BAR();
;     { const int tk_ = k0; k0 = k1; k1 = k2; k2 = tk_; const int tv_ = v0; v0 = v1; v1 = v2; v2 = tv_; }
;   }
.LBB0_298:
	v_exp_f32_e32 v98, v98
	v_exp_f32_e32 v114, v114
	v_exp_f32_e32 v99, v99
	v_exp_f32_e32 v115, v115
	v_exp_f32_e32 v100, v100
	v_exp_f32_e32 v101, v101
	v_exp_f32_e32 v102, v102
	v_exp_f32_e32 v103, v103
	v_exp_f32_e32 v106, v106
	v_exp_f32_e32 v107, v107
	v_exp_f32_e32 v116, v116
	v_exp_f32_e32 v117, v117
	v_exp_f32_e32 v118, v118
	v_exp_f32_e32 v119, v119
	v_exp_f32_e32 v104, v104
	v_exp_f32_e32 v120, v120
	v_exp_f32_e32 v105, v105
	v_exp_f32_e32 v121, v121
	v_exp_f32_e32 v122, v122
	v_exp_f32_e32 v123, v123
	v_exp_f32_e32 v108, v108
	v_exp_f32_e32 v124, v124
	v_exp_f32_e32 v109, v109
	v_exp_f32_e32 v125, v125
	v_exp_f32_e32 v110, v110
	v_exp_f32_e32 v126, v126
	v_exp_f32_e32 v111, v111
	v_exp_f32_e32 v127, v127
	v_exp_f32_e32 v112, v112
	v_exp_f32_e32 v128, v128
	v_exp_f32_e32 v113, v113
	v_exp_f32_e32 v129, v129
	v_cvt_pk_bf16_f32 v18, v98, v99
	v_cvt_pk_bf16_f32 v19, v100, v101
	v_cvt_pk_bf16_f32 v20, v102, v103
	v_cvt_pk_bf16_f32 v22, v106, v107
	v_cvt_pk_bf16_f32 v26, v114, v115
	v_cvt_pk_bf16_f32 v21, v104, v105
	v_cvt_pk_bf16_f32 v23, v108, v109
	v_cvt_pk_bf16_f32 v24, v110, v111
	v_cvt_pk_bf16_f32 v25, v112, v113
	v_cvt_pk_bf16_f32 v27, v116, v117
	v_cvt_pk_bf16_f32 v28, v118, v119
	v_cvt_pk_bf16_f32 v29, v120, v121
	v_cvt_pk_bf16_f32 v30, v122, v123
	v_cvt_pk_bf16_f32 v31, v124, v125
	v_cvt_pk_bf16_f32 v32, v126, v127
	v_cvt_pk_bf16_f32 v33, v128, v129
	s_waitcnt vmcnt(0)
	ds_write_b128 v248, v[224:227] offset:16384
	ds_write_b128 v168, v[228:231] offset:32768
	ds_write_b128 v169, v[232:235] offset:32768
	ds_read_b128 v[152:155], v249 offset:34816
	ds_read_b128 v[156:159], v249 offset:39424
	ds_read_b128 v[160:163], v249 offset:34848
	ds_read_b128 v[176:179], v249 offset:39456
	s_waitcnt lgkmcnt(4)
	s_barrier
	s_setprio 2
	s_waitcnt lgkmcnt(3)
	v_mfma_f32_32x32x16_bf16 v[98:113], v[152:155], v[136:139], v[82:97]
	ds_read_b128 v[180:183], v249 offset:34880
	s_waitcnt lgkmcnt(3)
	v_mfma_f32_32x32x16_bf16 v[114:129], v[156:159], v[136:139], v[82:97]
	ds_read_b128 v[186:189], v249 offset:39488
	s_waitcnt lgkmcnt(3)
	v_mfma_f32_32x32x16_bf16 v[98:113], v[160:163], v[140:143], v[98:113]
	ds_read_b128 v[190:193], v249 offset:34912
	ds_read_b64_tr_b16 v[198:199], v131 offset:16384
	ds_read_b64_tr_b16 v[200:201], v131 offset:18432
	s_waitcnt lgkmcnt(5)
	v_mfma_f32_32x32x16_bf16 v[114:129], v[176:179], v[140:143], v[114:129]
	ds_read_b128 v[194:197], v249 offset:39520
	ds_read_b64_tr_b16 v[212:213], v131 offset:20480
	ds_read_b64_tr_b16 v[214:215], v131 offset:22528
	s_waitcnt lgkmcnt(7)
	v_mfma_f32_32x32x16_bf16 v[98:113], v[180:183], v[144:147], v[98:113]
	ds_read_b64_tr_b16 v[216:217], v131 offset:24576
	ds_read_b64_tr_b16 v[218:219], v131 offset:26624
	s_waitcnt lgkmcnt(8)
	v_mfma_f32_32x32x16_bf16 v[114:129], v[186:189], v[144:147], v[114:129]
	ds_read_b64_tr_b16 v[220:221], v131 offset:28672
	ds_read_b64_tr_b16 v[222:223], v131 offset:30720
	s_waitcnt lgkmcnt(9)
	v_mfma_f32_32x32x16_bf16 v[98:113], v[190:193], v[148:151], v[98:113]
	s_waitcnt lgkmcnt(6)
	v_mfma_f32_32x32x16_bf16 v[114:129], v[194:197], v[148:151], v[114:129]
	v_mfma_f32_32x32x16_bf16 v[66:81], v[18:21], v[198:201], v[66:81]
	ds_read_b64_tr_b16 v[236:237], v131 offset:16896
	ds_read_b64_tr_b16 v[238:239], v131 offset:18944
	s_waitcnt lgkmcnt(6)
	v_mfma_f32_32x32x16_bf16 v[66:81], v[22:25], v[212:215], v[66:81]
	ds_read_b64_tr_b16 v[198:199], v131 offset:20992
	ds_read_b64_tr_b16 v[200:201], v131 offset:23040
	s_waitcnt lgkmcnt(6)
	v_mfma_f32_32x32x16_bf16 v[66:81], v[26:29], v[216:219], v[66:81]
	ds_read_b64_tr_b16 v[212:213], v131 offset:25088
	ds_read_b64_tr_b16 v[214:215], v131 offset:27136
	s_waitcnt lgkmcnt(6)
	v_mfma_f32_32x32x16_bf16 v[66:81], v[30:33], v[220:223], v[66:81]
	ds_read_b64_tr_b16 v[216:217], v131 offset:29184
	ds_read_b64_tr_b16 v[218:219], v131 offset:31232
	v_max3_f32 v152, v98, v99, v100
	s_waitcnt lgkmcnt(6)
	v_mfma_f32_32x32x16_bf16 v[50:65], v[18:21], v[236:239], v[50:65]
	ds_read_b64_tr_b16 v[220:221], v131 offset:17408
	ds_read_b64_tr_b16 v[222:223], v131 offset:19456
	v_max3_f32 v174, v114, v115, v116
	s_waitcnt lgkmcnt(6)
	v_mfma_f32_32x32x16_bf16 v[50:65], v[22:25], v[198:201], v[50:65]
	ds_read_b64_tr_b16 v[236:237], v131 offset:21504
	ds_read_b64_tr_b16 v[238:239], v131 offset:23552
	v_max3_f32 v152, v152, v101, v102
	s_waitcnt lgkmcnt(6)
	v_mfma_f32_32x32x16_bf16 v[50:65], v[26:29], v[212:215], v[50:65]
	ds_read_b64_tr_b16 v[198:199], v131 offset:25600
	ds_read_b64_tr_b16 v[200:201], v131 offset:27648
	v_max3_f32 v174, v174, v117, v118
	s_waitcnt lgkmcnt(6)
	v_mfma_f32_32x32x16_bf16 v[50:65], v[30:33], v[216:219], v[50:65]
	ds_read_b64_tr_b16 v[212:213], v131 offset:29696
	ds_read_b64_tr_b16 v[214:215], v131 offset:31744
	v_max3_f32 v152, v152, v103, v104
	s_waitcnt lgkmcnt(6)
	v_mfma_f32_32x32x16_bf16 v[34:49], v[18:21], v[220:223], v[34:49]
	ds_read_b64_tr_b16 v[216:217], v131 offset:17920
	ds_read_b64_tr_b16 v[218:219], v131 offset:19968
	v_max3_f32 v174, v174, v119, v120
	s_waitcnt lgkmcnt(6)
	v_mfma_f32_32x32x16_bf16 v[34:49], v[22:25], v[236:239], v[34:49]
	ds_read_b64_tr_b16 v[220:221], v131 offset:22016
	ds_read_b64_tr_b16 v[222:223], v131 offset:24064
	v_max3_f32 v152, v152, v105, v106
	s_waitcnt lgkmcnt(6)
	v_mfma_f32_32x32x16_bf16 v[34:49], v[26:29], v[198:201], v[34:49]
	ds_read_b64_tr_b16 v[236:237], v131 offset:26112
	ds_read_b64_tr_b16 v[238:239], v131 offset:28160
	v_max3_f32 v174, v174, v121, v122
	s_waitcnt lgkmcnt(6)
	v_mfma_f32_32x32x16_bf16 v[34:49], v[30:33], v[212:215], v[34:49]
	ds_read_b64_tr_b16 v[198:199], v131 offset:30208
	ds_read_b64_tr_b16 v[200:201], v131 offset:32256
	v_max3_f32 v152, v152, v107, v108
	s_waitcnt lgkmcnt(6)
	v_mfma_f32_32x32x16_bf16 v[2:17], v[18:21], v[216:219], v[2:17]
	v_max3_f32 v174, v174, v123, v124
	s_min_u32 s14, s90, 0x7c
	s_lshl_b32 s14, s14, 17
	s_add_i32 s19, s14, 0x60000
	s_add_i32 s92, s36, 0xffff0000
	s_mov_b32 s14, s10
	s_mov_b32 s15, s11
	buffer_load_dwordx4 v[224:227], v171, s[8:11], s19 offen
	s_waitcnt lgkmcnt(4)
	v_mfma_f32_32x32x16_bf16 v[2:17], v[22:25], v[220:223], v[2:17]
	v_max3_f32 v152, v152, v109, v110
	buffer_load_dwordx4 v[228:231], v172, s[12:15], s92 offen
	s_waitcnt lgkmcnt(2)
	v_mfma_f32_32x32x16_bf16 v[2:17], v[26:29], v[236:239], v[2:17]
	v_max3_f32 v174, v174, v125, v126
	buffer_load_dwordx4 v[232:235], v172, s[12:15], s36 offen
	s_add_i32 s36, s36, 0x20000
	s_add_i32 s90, s90, 1
	s_cmpk_eq_i32 s90, 0x7e
	s_waitcnt lgkmcnt(0)
	v_mfma_f32_32x32x16_bf16 v[2:17], v[30:33], v[198:201], v[2:17]
	v_max3_f32 v152, v152, v111, v112
	v_mfma_f32_16x16x32_bf16 v[240:243], v[18:21], v[132:135], v[240:243]
	v_max3_f32 v174, v174, v127, v128
	v_mfma_f32_16x16x32_bf16 v[240:243], v[22:25], v[132:135], v[240:243]
	v_max_f32 v152, v152, v113
	v_mfma_f32_16x16x32_bf16 v[240:243], v[26:29], v[132:135], v[240:243]
	v_max_f32 v174, v174, v129
	v_mfma_f32_16x16x32_bf16 v[240:243], v[30:33], v[132:135], v[240:243]
	v_max_f32 v174, v174, v152
	s_setprio 0
	s_barrier
	s_cbranch_scc1 .Lu3_exit_b2_0

; #define ATT_SBAR() __builtin_amdgcn_sched_barrier(0)
; __device__ __forceinline__ unsigned cvtpk(float lo, float hi) { f32x2_t v = {lo, hi}; bf16x2_t b = __builtin_convertvector(v, bf16x2_t); return __builtin_bit_cast(unsigned, b); }
; #define ATT_LOAD_K(t) do { const unsigned so_ = (unsigned)(t) * (unsigned)(KVBLK * LDK * 2); sk0 = __builtin_bit_cast(bf16x8, __builtin_amdgcn_raw_buffer_load_b128(krs, koff, so_, 0)); \
;     if constexpr (DQK == 128) sk1 = __builtin_bit_cast(bf16x8, __builtin_amdgcn_raw_buffer_load_b128(krs, koff, so_ + (unsigned)(32 * LDK * 2), 0)); } while (0)
; #define ATT_LOAD_V(t) do { const unsigned so_ = (unsigned)(t) * (unsigned)(KVBLK * LDV * 2); sv0 = __builtin_bit_cast(bf16x8, __builtin_amdgcn_raw_buffer_load_b128(vrs, voff, so_, 0)); \
;     sv1 = __builtin_bit_cast(bf16x8, __builtin_amdgcn_raw_buffer_load_b128(vrs, voff, so_ + (unsigned)(32 * LDV * 2), 0)); } while (0)
; #define ATT_WRITE_K(so) do { *(bf16x8*)(K_lds + (so) + kswz<DQK>(kr, kc * 2)) = sk0; if constexpr (DQK == 128) *(bf16x8*)(K_lds + (so) + kswz<DQK>(32 + kr, kc * 2)) = sk1; } while (0)
;     ...
;   for (int t = 0; t + 1 < NT; ++t) {
;     if constexpr (ABL & 1) { u32x4 w0 = {cvtpk(p0[0], p0[1]), cvtpk(p0[2], p0[3]), cvtpk(p0[4], p0[5]), cvtpk(p0[6], p0[7])}, w1 = {cvtpk(p0[8], p0[9]), cvtpk(p0[10], p0[11]), cvtpk(p0[12], p0[13]), cvtpk(p0[14], p0[15])};
;         u32x4 w2 = {cvtpk(p1[0], p1[1]), cvtpk(p1[2], p1[3]), cvtpk(p1[4], p1[5]), cvtpk(p1[6], p1[7])}, w3 = {cvtpk(p1[8], p1[9]), cvtpk(p1[10], p1[11]), cvtpk(p1[12], p1[13]), cvtpk(p1[14], p1[15])};
;         pa0 = *reinterpret_cast<bf16x8*>(&w0); pa1 = *reinterpret_cast<bf16x8*>(&w1); pa2 = *reinterpret_cast<bf16x8*>(&w2); pa3 = *reinterpret_cast<bf16x8*>(&w3); }
;     else { ATT_SOFTMAX(t == 0); }
;     if constexpr (!(ABL & 4)) { ATT_WRITE_K(k2); ATT_WRITE_V(v1); }
;     ATT_SBAR();
; #pragma unroll
;     for (int ks = 0; ks < 4; ++ks) ATT_VPAIR(va, v0, 0, ks);
;     asm volatile("s_waitcnt lgkmcnt(8)" ::: "memory"); ATT_BAR();
;     ATT_XSECTION(true);
;     if constexpr (!(ABL & 4)) { const int tk = (t + 3 < NT) ? t + 3 : NT - 1, tv = (t + 2 < NT) ? t + 2 : NT - 1; ATT_LOAD_K(tk); ATT_LOAD_V(tv); }
;     ATT_BAR();
;     { const int tk_ = k0; k0 = k1; k1 = k2; k2 = tk_; const int tv_ = v0; v0 = v1; v1 = v2; v2 = tv_; }
;   }
.Lu3_join_b2_1:
	v_exp_f32_e32 v98, v98
	v_exp_f32_e32 v114, v114
	v_exp_f32_e32 v99, v99
	v_exp_f32_e32 v115, v115
	v_exp_f32_e32 v100, v100
	v_exp_f32_e32 v101, v101
	v_exp_f32_e32 v102, v102
	v_exp_f32_e32 v103, v103
	v_exp_f32_e32 v106, v106
	v_exp_f32_e32 v107, v107
	v_exp_f32_e32 v116, v116
	v_exp_f32_e32 v117, v117
	v_exp_f32_e32 v118, v118
	v_exp_f32_e32 v119, v119
	v_exp_f32_e32 v104, v104
	v_exp_f32_e32 v120, v120
	v_exp_f32_e32 v105, v105
	v_exp_f32_e32 v121, v121
	v_exp_f32_e32 v122, v122
	v_exp_f32_e32 v123, v123
	v_exp_f32_e32 v108, v108
	v_exp_f32_e32 v124, v124
	v_exp_f32_e32 v109, v109
	v_exp_f32_e32 v125, v125
	v_exp_f32_e32 v110, v110
	v_exp_f32_e32 v126, v126
	v_exp_f32_e32 v111, v111
	v_exp_f32_e32 v127, v127
	v_exp_f32_e32 v112, v112
	v_exp_f32_e32 v128, v128
	v_exp_f32_e32 v113, v113
	v_exp_f32_e32 v129, v129
	v_cvt_pk_bf16_f32 v18, v98, v99
	v_cvt_pk_bf16_f32 v19, v100, v101
	v_cvt_pk_bf16_f32 v20, v102, v103
	v_cvt_pk_bf16_f32 v22, v106, v107
	v_cvt_pk_bf16_f32 v26, v114, v115
	v_cvt_pk_bf16_f32 v21, v104, v105
	v_cvt_pk_bf16_f32 v23, v108, v109
	v_cvt_pk_bf16_f32 v24, v110, v111
	v_cvt_pk_bf16_f32 v25, v112, v113
	v_cvt_pk_bf16_f32 v27, v116, v117
	v_cvt_pk_bf16_f32 v28, v118, v119
	v_cvt_pk_bf16_f32 v29, v120, v121
	v_cvt_pk_bf16_f32 v30, v122, v123
	v_cvt_pk_bf16_f32 v31, v124, v125
	v_cvt_pk_bf16_f32 v32, v126, v127
	v_cvt_pk_bf16_f32 v33, v128, v129
	s_waitcnt vmcnt(0)
	ds_write_b128 v248, v[224:227] offset:25600
	ds_write_b128 v168, v[228:231]
	ds_write_b128 v169, v[232:235]
	ds_read_b128 v[152:155], v249 offset:16384
	ds_read_b128 v[156:159], v249 offset:20992
	ds_read_b128 v[160:163], v249 offset:16416
	ds_read_b128 v[176:179], v249 offset:21024
	s_waitcnt lgkmcnt(4)
	s_barrier
	s_setprio 2
	s_waitcnt lgkmcnt(3)
	v_mfma_f32_32x32x16_bf16 v[98:113], v[152:155], v[136:139], v[82:97]
	ds_read_b128 v[180:183], v249 offset:16448
	s_waitcnt lgkmcnt(3)
	v_mfma_f32_32x32x16_bf16 v[114:129], v[156:159], v[136:139], v[82:97]
	ds_read_b128 v[186:189], v249 offset:21056
	s_waitcnt lgkmcnt(3)
	v_mfma_f32_32x32x16_bf16 v[98:113], v[160:163], v[140:143], v[98:113]
	ds_read_b128 v[190:193], v249 offset:16480
	ds_read_b64_tr_b16 v[198:199], v131 offset:32768
	ds_read_b64_tr_b16 v[200:201], v131 offset:34816
	s_waitcnt lgkmcnt(5)
	v_mfma_f32_32x32x16_bf16 v[114:129], v[176:179], v[140:143], v[114:129]
	ds_read_b128 v[194:197], v249 offset:21088
	ds_read_b64_tr_b16 v[212:213], v131 offset:36864
	ds_read_b64_tr_b16 v[214:215], v131 offset:38912
	s_waitcnt lgkmcnt(7)
	v_mfma_f32_32x32x16_bf16 v[98:113], v[180:183], v[144:147], v[98:113]
	ds_read_b64_tr_b16 v[216:217], v131 offset:40960
	ds_read_b64_tr_b16 v[218:219], v131 offset:43008
	s_waitcnt lgkmcnt(8)
	v_mfma_f32_32x32x16_bf16 v[114:129], v[186:189], v[144:147], v[114:129]
	ds_read_b64_tr_b16 v[220:221], v131 offset:45056
	ds_read_b64_tr_b16 v[222:223], v131 offset:47104
	s_waitcnt lgkmcnt(9)
	v_mfma_f32_32x32x16_bf16 v[98:113], v[190:193], v[148:151], v[98:113]
	s_waitcnt lgkmcnt(6)
	v_mfma_f32_32x32x16_bf16 v[114:129], v[194:197], v[148:151], v[114:129]
	v_mfma_f32_32x32x16_bf16 v[66:81], v[18:21], v[198:201], v[66:81]
	ds_read_b64_tr_b16 v[236:237], v131 offset:33280
	ds_read_b64_tr_b16 v[238:239], v131 offset:35328
	s_waitcnt lgkmcnt(6)
	v_mfma_f32_32x32x16_bf16 v[66:81], v[22:25], v[212:215], v[66:81]
	ds_read_b64_tr_b16 v[198:199], v131 offset:37376
	ds_read_b64_tr_b16 v[200:201], v131 offset:39424
	s_waitcnt lgkmcnt(6)
	v_mfma_f32_32x32x16_bf16 v[66:81], v[26:29], v[216:219], v[66:81]
	ds_read_b64_tr_b16 v[212:213], v131 offset:41472
	ds_read_b64_tr_b16 v[214:215], v131 offset:43520
	s_waitcnt lgkmcnt(6)
	v_mfma_f32_32x32x16_bf16 v[66:81], v[30:33], v[220:223], v[66:81]
	ds_read_b64_tr_b16 v[216:217], v131 offset:45568
	ds_read_b64_tr_b16 v[218:219], v131 offset:47616
	v_max3_f32 v152, v98, v99, v100
	s_waitcnt lgkmcnt(6)
	v_mfma_f32_32x32x16_bf16 v[50:65], v[18:21], v[236:239], v[50:65]
	ds_read_b64_tr_b16 v[220:221], v131 offset:33792
	ds_read_b64_tr_b16 v[222:223], v131 offset:35840
	v_max3_f32 v174, v114, v115, v116
	s_waitcnt lgkmcnt(6)
	v_mfma_f32_32x32x16_bf16 v[50:65], v[22:25], v[198:201], v[50:65]
	ds_read_b64_tr_b16 v[236:237], v131 offset:37888
	ds_read_b64_tr_b16 v[238:239], v131 offset:39936
	v_max3_f32 v152, v152, v101, v102
	s_waitcnt lgkmcnt(6)
	v_mfma_f32_32x32x16_bf16 v[50:65], v[26:29], v[212:215], v[50:65]
	ds_read_b64_tr_b16 v[198:199], v131 offset:41984
	ds_read_b64_tr_b16 v[200:201], v131 offset:44032
	v_max3_f32 v174, v174, v117, v118
	s_waitcnt lgkmcnt(6)
	v_mfma_f32_32x32x16_bf16 v[50:65], v[30:33], v[216:219], v[50:65]
	ds_read_b64_tr_b16 v[212:213], v131 offset:46080
	ds_read_b64_tr_b16 v[214:215], v131 offset:48128
	v_max3_f32 v152, v152, v103, v104
	s_waitcnt lgkmcnt(6)
	v_mfma_f32_32x32x16_bf16 v[34:49], v[18:21], v[220:223], v[34:49]
	ds_read_b64_tr_b16 v[216:217], v131 offset:34304
	ds_read_b64_tr_b16 v[218:219], v131 offset:36352
	v_max3_f32 v174, v174, v119, v120
	s_waitcnt lgkmcnt(6)
	v_mfma_f32_32x32x16_bf16 v[34:49], v[22:25], v[236:239], v[34:49]
	ds_read_b64_tr_b16 v[220:221], v131 offset:38400
	ds_read_b64_tr_b16 v[222:223], v131 offset:40448
	v_max3_f32 v152, v152, v105, v106
	s_waitcnt lgkmcnt(6)
	v_mfma_f32_32x32x16_bf16 v[34:49], v[26:29], v[198:201], v[34:49]
	ds_read_b64_tr_b16 v[236:237], v131 offset:42496
	ds_read_b64_tr_b16 v[238:239], v131 offset:44544
	v_max3_f32 v174, v174, v121, v122
	s_waitcnt lgkmcnt(6)
	v_mfma_f32_32x32x16_bf16 v[34:49], v[30:33], v[212:215], v[34:49]
	ds_read_b64_tr_b16 v[198:199], v131 offset:46592
	ds_read_b64_tr_b16 v[200:201], v131 offset:48640
	v_max3_f32 v152, v152, v107, v108
	s_waitcnt lgkmcnt(6)
	v_mfma_f32_32x32x16_bf16 v[2:17], v[18:21], v[216:219], v[2:17]
	v_max3_f32 v174, v174, v123, v124
	s_min_u32 s14, s90, 0x7c
	s_lshl_b32 s14, s14, 17
	s_add_i32 s19, s14, 0x60000
	s_add_i32 s92, s36, 0xffff0000
	s_mov_b32 s14, s10
	s_mov_b32 s15, s11
	buffer_load_dwordx4 v[224:227], v171, s[8:11], s19 offen
	s_waitcnt lgkmcnt(4)
	v_mfma_f32_32x32x16_bf16 v[2:17], v[22:25], v[220:223], v[2:17]
	v_max3_f32 v152, v152, v109, v110
	buffer_load_dwordx4 v[228:231], v172, s[12:15], s92 offen
	s_waitcnt lgkmcnt(2)
	v_mfma_f32_32x32x16_bf16 v[2:17], v[26:29], v[236:239], v[2:17]
	v_max3_f32 v174, v174, v125, v126
	buffer_load_dwordx4 v[232:235], v172, s[12:15], s36 offen
	s_add_i32 s36, s36, 0x20000
	s_add_i32 s90, s90, 1
	s_cmpk_eq_i32 s90, 0x7e
	s_waitcnt lgkmcnt(0)
	v_mfma_f32_32x32x16_bf16 v[2:17], v[30:33], v[198:201], v[2:17]
	v_max3_f32 v152, v152, v111, v112
	v_mfma_f32_16x16x32_bf16 v[240:243], v[18:21], v[132:135], v[240:243]
	v_max3_f32 v174, v174, v127, v128
	v_mfma_f32_16x16x32_bf16 v[240:243], v[22:25], v[132:135], v[240:243]
	v_max_f32 v152, v152, v113
	v_mfma_f32_16x16x32_bf16 v[240:243], v[26:29], v[132:135], v[240:243]
	v_max_f32 v174, v174, v129
	v_mfma_f32_16x16x32_bf16 v[240:243], v[30:33], v[132:135], v[240:243]
	v_max_f32 v174, v174, v152
	s_setprio 0
	s_barrier
	s_cbranch_scc1 .Lu3_exit_b2_1

; #define ATT_SBAR() __builtin_amdgcn_sched_barrier(0)
; __device__ __forceinline__ unsigned cvtpk(float lo, float hi) { f32x2_t v = {lo, hi}; bf16x2_t b = __builtin_convertvector(v, bf16x2_t); return __builtin_bit_cast(unsigned, b); }
; #define ATT_LOAD_K(t) do { const unsigned so_ = (unsigned)(t) * (unsigned)(KVBLK * LDK * 2); sk0 = __builtin_bit_cast(bf16x8, __builtin_amdgcn_raw_buffer_load_b128(krs, koff, so_, 0)); \
;     if constexpr (DQK == 128) sk1 = __builtin_bit_cast(bf16x8, __builtin_amdgcn_raw_buffer_load_b128(krs, koff, so_ + (unsigned)(32 * LDK * 2), 0)); } while (0)
; #define ATT_LOAD_V(t) do { const unsigned so_ = (unsigned)(t) * (unsigned)(KVBLK * LDV * 2); sv0 = __builtin_bit_cast(bf16x8, __builtin_amdgcn_raw_buffer_load_b128(vrs, voff, so_, 0)); \
;     sv1 = __builtin_bit_cast(bf16x8, __builtin_amdgcn_raw_buffer_load_b128(vrs, voff, so_ + (unsigned)(32 * LDV * 2), 0)); } while (0)
; #define ATT_WRITE_K(so) do { *(bf16x8*)(K_lds + (so) + kswz<DQK>(kr, kc * 2)) = sk0; if constexpr (DQK == 128) *(bf16x8*)(K_lds + (so) + kswz<DQK>(32 + kr, kc * 2)) = sk1; } while (0)
;     ...
;   for (int t = 0; t + 1 < NT; ++t) {
;     if constexpr (ABL & 1) { u32x4 w0 = {cvtpk(p0[0], p0[1]), cvtpk(p0[2], p0[3]), cvtpk(p0[4], p0[5]), cvtpk(p0[6], p0[7])}, w1 = {cvtpk(p0[8], p0[9]), cvtpk(p0[10], p0[11]), cvtpk(p0[12], p0[13]), cvtpk(p0[14], p0[15])};
;         u32x4 w2 = {cvtpk(p1[0], p1[1]), cvtpk(p1[2], p1[3]), cvtpk(p1[4], p1[5]), cvtpk(p1[6], p1[7])}, w3 = {cvtpk(p1[8], p1[9]), cvtpk(p1[10], p1[11]), cvtpk(p1[12], p1[13]), cvtpk(p1[14], p1[15])};
;         pa0 = *reinterpret_cast<bf16x8*>(&w0); pa1 = *reinterpret_cast<bf16x8*>(&w1); pa2 = *reinterpret_cast<bf16x8*>(&w2); pa3 = *reinterpret_cast<bf16x8*>(&w3); }
;     else { ATT_SOFTMAX(t == 0); }
;     if constexpr (!(ABL & 4)) { ATT_WRITE_K(k2); ATT_WRITE_V(v1); }
;     ATT_SBAR();
; #pragma unroll
;     for (int ks = 0; ks < 4; ++ks) ATT_VPAIR(va, v0, 0, ks);
;     asm volatile("s_waitcnt lgkmcnt(8)" ::: "memory"); ATT_BAR();
;     ATT_XSECTION(true);
;     if constexpr (!(ABL & 4)) { const int tk = (t + 3 < NT) ? t + 3 : NT - 1, tv = (t + 2 < NT) ? t + 2 : NT - 1; ATT_LOAD_K(tk); ATT_LOAD_V(tv); }
;     ATT_BAR();
;     { const int tk_ = k0; k0 = k1; k1 = k2; k2 = tk_; const int tv_ = v0; v0 = v1; v1 = v2; v2 = tv_; }
;   }
.Lu3_join_b2_2:
	v_exp_f32_e32 v98, v98
	v_exp_f32_e32 v114, v114
	v_exp_f32_e32 v99, v99
	v_exp_f32_e32 v115, v115
	v_exp_f32_e32 v100, v100
	v_exp_f32_e32 v101, v101
	v_exp_f32_e32 v102, v102
	v_exp_f32_e32 v103, v103
	v_exp_f32_e32 v106, v106
	v_exp_f32_e32 v107, v107
	v_exp_f32_e32 v116, v116
	v_exp_f32_e32 v117, v117
	v_exp_f32_e32 v118, v118
	v_exp_f32_e32 v119, v119
	v_exp_f32_e32 v104, v104
	v_exp_f32_e32 v120, v120
	v_exp_f32_e32 v105, v105
	v_exp_f32_e32 v121, v121
	v_exp_f32_e32 v122, v122
	v_exp_f32_e32 v123, v123
	v_exp_f32_e32 v108, v108
	v_exp_f32_e32 v124, v124
	v_exp_f32_e32 v109, v109
	v_exp_f32_e32 v125, v125
	v_exp_f32_e32 v110, v110
	v_exp_f32_e32 v126, v126
	v_exp_f32_e32 v111, v111
	v_exp_f32_e32 v127, v127
	v_exp_f32_e32 v112, v112
	v_exp_f32_e32 v128, v128
	v_exp_f32_e32 v113, v113
	v_exp_f32_e32 v129, v129
	v_cvt_pk_bf16_f32 v18, v98, v99
	v_cvt_pk_bf16_f32 v19, v100, v101
	v_cvt_pk_bf16_f32 v20, v102, v103
	v_cvt_pk_bf16_f32 v22, v106, v107
	v_cvt_pk_bf16_f32 v26, v114, v115
	v_cvt_pk_bf16_f32 v21, v104, v105
	v_cvt_pk_bf16_f32 v23, v108, v109
	v_cvt_pk_bf16_f32 v24, v110, v111
	v_cvt_pk_bf16_f32 v25, v112, v113
	v_cvt_pk_bf16_f32 v27, v116, v117
	v_cvt_pk_bf16_f32 v28, v118, v119
	v_cvt_pk_bf16_f32 v29, v120, v121
	v_cvt_pk_bf16_f32 v30, v122, v123
	v_cvt_pk_bf16_f32 v31, v124, v125
	v_cvt_pk_bf16_f32 v32, v126, v127
	v_cvt_pk_bf16_f32 v33, v128, v129
	s_waitcnt vmcnt(0)
	ds_write_b128 v248, v[224:227] offset:34816
	ds_write_b128 v168, v[228:231] offset:16384
	ds_write_b128 v169, v[232:235] offset:16384
	ds_read_b128 v[152:155], v249 offset:25600
	ds_read_b128 v[156:159], v249 offset:30208
	ds_read_b128 v[160:163], v249 offset:25632
	ds_read_b128 v[176:179], v249 offset:30240
	s_waitcnt lgkmcnt(4)
	s_barrier
	s_setprio 2
	s_waitcnt lgkmcnt(3)
	v_mfma_f32_32x32x16_bf16 v[98:113], v[152:155], v[136:139], v[82:97]
	ds_read_b128 v[180:183], v249 offset:25664
	s_waitcnt lgkmcnt(3)
	v_mfma_f32_32x32x16_bf16 v[114:129], v[156:159], v[136:139], v[82:97]
	ds_read_b128 v[186:189], v249 offset:30272
	s_waitcnt lgkmcnt(3)
	v_mfma_f32_32x32x16_bf16 v[98:113], v[160:163], v[140:143], v[98:113]
	ds_read_b128 v[190:193], v249 offset:25696
	ds_read_b64_tr_b16 v[198:199], v131
	ds_read_b64_tr_b16 v[200:201], v131 offset:2048
	s_waitcnt lgkmcnt(5)
	v_mfma_f32_32x32x16_bf16 v[114:129], v[176:179], v[140:143], v[114:129]
	ds_read_b128 v[194:197], v249 offset:30304
	ds_read_b64_tr_b16 v[212:213], v131 offset:4096
	ds_read_b64_tr_b16 v[214:215], v131 offset:6144
	s_waitcnt lgkmcnt(7)
	v_mfma_f32_32x32x16_bf16 v[98:113], v[180:183], v[144:147], v[98:113]
	ds_read_b64_tr_b16 v[216:217], v131 offset:8192
	ds_read_b64_tr_b16 v[218:219], v131 offset:10240
	s_waitcnt lgkmcnt(8)
	v_mfma_f32_32x32x16_bf16 v[114:129], v[186:189], v[144:147], v[114:129]
	ds_read_b64_tr_b16 v[220:221], v131 offset:12288
	ds_read_b64_tr_b16 v[222:223], v131 offset:14336
	s_waitcnt lgkmcnt(9)
	v_mfma_f32_32x32x16_bf16 v[98:113], v[190:193], v[148:151], v[98:113]
	s_waitcnt lgkmcnt(6)
	v_mfma_f32_32x32x16_bf16 v[114:129], v[194:197], v[148:151], v[114:129]
	v_mfma_f32_32x32x16_bf16 v[66:81], v[18:21], v[198:201], v[66:81]
	ds_read_b64_tr_b16 v[236:237], v131 offset:512
	ds_read_b64_tr_b16 v[238:239], v131 offset:2560
	s_waitcnt lgkmcnt(6)
	v_mfma_f32_32x32x16_bf16 v[66:81], v[22:25], v[212:215], v[66:81]
	ds_read_b64_tr_b16 v[198:199], v131 offset:4608
	ds_read_b64_tr_b16 v[200:201], v131 offset:6656
	s_waitcnt lgkmcnt(6)
	v_mfma_f32_32x32x16_bf16 v[66:81], v[26:29], v[216:219], v[66:81]
	ds_read_b64_tr_b16 v[212:213], v131 offset:8704
	ds_read_b64_tr_b16 v[214:215], v131 offset:10752
	s_waitcnt lgkmcnt(6)
	v_mfma_f32_32x32x16_bf16 v[66:81], v[30:33], v[220:223], v[66:81]
	ds_read_b64_tr_b16 v[216:217], v131 offset:12800
	ds_read_b64_tr_b16 v[218:219], v131 offset:14848
	v_max3_f32 v152, v98, v99, v100
	s_waitcnt lgkmcnt(6)
	v_mfma_f32_32x32x16_bf16 v[50:65], v[18:21], v[236:239], v[50:65]
	ds_read_b64_tr_b16 v[220:221], v131 offset:1024
	ds_read_b64_tr_b16 v[222:223], v131 offset:3072
	v_max3_f32 v174, v114, v115, v116
	s_waitcnt lgkmcnt(6)
	v_mfma_f32_32x32x16_bf16 v[50:65], v[22:25], v[198:201], v[50:65]
	ds_read_b64_tr_b16 v[236:237], v131 offset:5120
	ds_read_b64_tr_b16 v[238:239], v131 offset:7168
	v_max3_f32 v152, v152, v101, v102
	s_waitcnt lgkmcnt(6)
	v_mfma_f32_32x32x16_bf16 v[50:65], v[26:29], v[212:215], v[50:65]
	ds_read_b64_tr_b16 v[198:199], v131 offset:9216
	ds_read_b64_tr_b16 v[200:201], v131 offset:11264
	v_max3_f32 v174, v174, v117, v118
	s_waitcnt lgkmcnt(6)
	v_mfma_f32_32x32x16_bf16 v[50:65], v[30:33], v[216:219], v[50:65]
	ds_read_b64_tr_b16 v[212:213], v131 offset:13312
	ds_read_b64_tr_b16 v[214:215], v131 offset:15360
	v_max3_f32 v152, v152, v103, v104
	s_waitcnt lgkmcnt(6)
	v_mfma_f32_32x32x16_bf16 v[34:49], v[18:21], v[220:223], v[34:49]
	ds_read_b64_tr_b16 v[216:217], v131 offset:1536
	ds_read_b64_tr_b16 v[218:219], v131 offset:3584
	v_max3_f32 v174, v174, v119, v120
	s_waitcnt lgkmcnt(6)
	v_mfma_f32_32x32x16_bf16 v[34:49], v[22:25], v[236:239], v[34:49]
	ds_read_b64_tr_b16 v[220:221], v131 offset:5632
	ds_read_b64_tr_b16 v[222:223], v131 offset:7680
	v_max3_f32 v152, v152, v105, v106
	s_waitcnt lgkmcnt(6)
	v_mfma_f32_32x32x16_bf16 v[34:49], v[26:29], v[198:201], v[34:49]
	ds_read_b64_tr_b16 v[236:237], v131 offset:9728
	ds_read_b64_tr_b16 v[238:239], v131 offset:11776
	v_max3_f32 v174, v174, v121, v122
	s_waitcnt lgkmcnt(6)
	v_mfma_f32_32x32x16_bf16 v[34:49], v[30:33], v[212:215], v[34:49]
	ds_read_b64_tr_b16 v[198:199], v131 offset:13824
	ds_read_b64_tr_b16 v[200:201], v131 offset:15872
	v_max3_f32 v152, v152, v107, v108
	s_waitcnt lgkmcnt(6)
	v_mfma_f32_32x32x16_bf16 v[2:17], v[18:21], v[216:219], v[2:17]
	v_max3_f32 v174, v174, v123, v124
	s_min_u32 s14, s90, 0x7c
	s_lshl_b32 s14, s14, 17
	s_add_i32 s19, s14, 0x60000
	s_add_i32 s92, s36, 0xffff0000
	s_mov_b32 s14, s10
	s_mov_b32 s15, s11
	buffer_load_dwordx4 v[224:227], v171, s[8:11], s19 offen
	s_waitcnt lgkmcnt(4)
	v_mfma_f32_32x32x16_bf16 v[2:17], v[22:25], v[220:223], v[2:17]
	v_max3_f32 v152, v152, v109, v110
	buffer_load_dwordx4 v[228:231], v172, s[12:15], s92 offen
	s_waitcnt lgkmcnt(2)
	v_mfma_f32_32x32x16_bf16 v[2:17], v[26:29], v[236:239], v[2:17]
	v_max3_f32 v174, v174, v125, v126
	buffer_load_dwordx4 v[232:235], v172, s[12:15], s36 offen
	s_add_i32 s36, s36, 0x20000
	s_add_i32 s90, s90, 1
	s_cmpk_eq_i32 s90, 0x7e
	s_waitcnt lgkmcnt(0)
	v_mfma_f32_32x32x16_bf16 v[2:17], v[30:33], v[198:201], v[2:17]
	v_max3_f32 v152, v152, v111, v112
	v_mfma_f32_16x16x32_bf16 v[240:243], v[18:21], v[132:135], v[240:243]
	v_max3_f32 v174, v174, v127, v128
	v_mfma_f32_16x16x32_bf16 v[240:243], v[22:25], v[132:135], v[240:243]
	v_max_f32 v152, v152, v113
	v_mfma_f32_16x16x32_bf16 v[240:243], v[26:29], v[132:135], v[240:243]
	v_max_f32 v174, v174, v129
	v_mfma_f32_16x16x32_bf16 v[240:243], v[30:33], v[132:135], v[240:243]
	v_max_f32 v174, v174, v152
	s_setprio 0
	s_barrier
	s_cbranch_scc1 .Lu3_exit_b2_2
	s_branch .Lu3_b2_0
